# v_final_b + P7 epilogue bias loads prefetched at the unit header into v240-255
# baseline (speedup 1.0000x reference)
.LBB0_984:
	s_ashr_i32 s98, s34, 3
	s_ashr_i32 s99, s98, 31
	s_lshl_b64 s[98:99], s[98:99], 13
	v_readlane_b32 s100, v239, 13
	v_readlane_b32 s101, v239, 14
	s_add_u32 s98, s100, s98
	s_addc_u32 s99, s101, s99
	s_lshl_b32 s100, s34, 7
	s_and_b32 s100, s100, 0x380
	v_or_b32_e32 v224, s100, v219
	v_lshlrev_b32_e32 v224, 2, v224
	global_load_dwordx4 v[240:243], v224, s[98:99]
	global_load_dwordx4 v[244:247], v224, s[98:99] offset:16
	s_add_u32 s98, s98, 0x1000
	s_addc_u32 s99, s99, 0
	global_load_dwordx4 v[248:251], v224, s[98:99]
	global_load_dwordx4 v[252:255], v224, s[98:99] offset:16
	s_ashr_i32 s11, s10, 31
	s_lshl_b64 s[30:31], s[10:11], 18
	s_add_u32 s30, s40, s30
	s_addc_u32 s31, s41, s31
	s_and_b64 s[46:47], s[36:37], exec
	s_cselect_b32 s2, s31, s39
	s_cselect_b32 s11, s30, s38
	s_xor_b32 s44, s44, 0x400
	s_add_i32 s82, s44, 0
	s_add_i32 s82, s82, 0x23400
	s_add_u32 s85, s38, 0x100
	s_addc_u32 s86, s39, 0
	s_mov_b32 s87, -2
	s_mov_b64 s[38:39], s[18:19]
	s_mov_b32 s88, 1
	s_branch .LBB0_986

.LBB0_994:
	s_ashr_i32 s36, s34, 3
	s_lshl_b32 s2, s34, 7
	s_ashr_i32 s37, s36, 31
	v_readlane_b32 s80, v239, 7
	s_and_b32 s2, s2, 0x380
	s_lshl_b64 s[36:37], s[36:37], 13
	v_readlane_b32 s86, v239, 13
	v_or_b32_e32 v2, s2, v219
	v_readlane_b32 s87, v239, 14
	s_add_u32 s36, s86, s36
	s_waitcnt vmcnt(0)
	s_addc_u32 s37, s87, s37
	v_lshlrev_b32_e32 v4, 2, v2
	v_mov_b32_e32 v5, v199
	v_mov_b32_e32 v26, v240
	v_mov_b32_e32 v27, v241
	v_mov_b32_e32 v28, v242
	v_mov_b32_e32 v29, v243
	v_mov_b32_e32 v30, v244
	v_mov_b32_e32 v31, v245
	v_mov_b32_e32 v32, v246
	v_mov_b32_e32 v33, v247
	v_lshl_add_u64 v[4:5], s[36:37], 0, v[4:5]
	s_mov_b64 s[36:37], 0x1000
	s_movk_i32 s2, 0x1000
	v_lshl_add_u64 v[6:7], v[4:5], 0, s[36:37]
	v_add_co_u32_e32 v4, vcc, s2, v4
	v_mov_b32_e32 v8, v186
	s_nop 0
	v_addc_co_u32_e32 v5, vcc, 0, v5, vcc
	v_mov_b32_e32 v34, v248
	v_mov_b32_e32 v35, v249
	v_mov_b32_e32 v36, v250
	v_mov_b32_e32 v37, v251
	v_mov_b32_e32 v38, v252
	v_mov_b32_e32 v39, v253
	v_mov_b32_e32 v40, v254
	v_mov_b32_e32 v41, v255
	v_mov_b32_e32 v6, v190
	v_mov_b32_e32 v14, v178
	v_mov_b32_e32 v24, v183
	v_mov_b32_e32 v20, v192
	v_lshl_add_u32 v4, s96, 8, v218
	v_ashrrev_i32_e32 v5, 31, v4
	v_lshlrev_b64 v[4:5], 10, v[4:5]
	v_mov_b32_e32 v3, v199
	v_mov_b32_e32 v12, v182
	v_mov_b32_e32 v42, v179
	v_mov_b32_e32 v22, v188
	v_lshl_add_u64 v[4:5], s[58:59], 0, v[4:5]
	v_lshl_add_u64 v[2:3], v[4:5], 0, v[2:3]
	v_lshl_add_u64 v[2:3], v[2:3], 0, v[204:205]
	s_mov_b32 s2, 0x8000
	v_readlane_b32 s81, v239, 8
	v_readlane_b32 s82, v239, 9
	v_readlane_b32 s83, v239, 10
	v_readlane_b32 s84, v239, 11
	v_readlane_b32 s85, v239, 12
	v_readlane_b32 s88, v239, 15
	v_readlane_b32 s89, v239, 16
	v_readlane_b32 s90, v239, 17
	v_readlane_b32 s91, v239, 18
	v_readlane_b32 s92, v239, 19
	v_readlane_b32 s93, v239, 20
	v_readlane_b32 s94, v239, 21
	v_readlane_b32 s95, v239, 22
	s_waitcnt vmcnt(0)
	v_mov_b32_e32 v7, v26
	v_mov_b32_e32 v9, v30
	v_pk_mul_f32 v[16:17], v[8:9], s[24:25]
	v_mov_b32_e32 v26, v191
	v_sub_f32_e32 v16, v16, v17
	v_mov_b32_e32 v21, v28
	v_pk_mul_f32 v[10:11], v[26:27], s[24:25]
	v_max_f32_e32 v16, 0xc1898193, v16
	v_pk_mul_f32 v[18:19], v[6:7], s[24:25]
	v_pk_mul_f32 v[6:7], v[20:21], s[24:25]
	v_add_f32_e32 v25, 1.0, v35
	v_add_f32_e32 v15, 1.0, v38
	v_sub_f32_e32 v10, v10, v11
	v_pk_mul_f32 v[20:21], v[14:15], s[26:27]
	v_pk_mul_f32 v[14:15], v[24:25], s[26:27]
	v_exp_f32_e32 v25, v16
	v_max_f32_e32 v10, 0xc1898193, v10
	v_sub_f32_e32 v18, v18, v19
	v_sub_f32_e32 v6, v6, v7
	v_exp_f32_e32 v26, v10
	v_sub_f32_e32 v14, v14, v15
	v_max_f32_e32 v18, 0xc1898193, v18
	v_max_f32_e32 v6, 0xc1898193, v6
	v_med3_f32 v14, v14, s71, v223
	v_mov_b32_e32 v30, v187
	v_mov_b32_e32 v23, v32
	v_add_f32_e32 v13, 1.0, v34
	v_add_f32_e32 v43, 1.0, v39
	v_exp_f32_e32 v24, v18
	v_sub_f32_e32 v20, v20, v21
	v_exp_f32_e32 v28, v6
	v_mul_f32_e32 v10, v10, v14
	v_add_f32_e32 v14, 1.0, v25
	v_pk_mul_f32 v[8:9], v[30:31], s[24:25]
	v_pk_mul_f32 v[4:5], v[22:23], s[24:25]
	v_pk_mul_f32 v[22:23], v[12:13], s[26:27]
	v_pk_mul_f32 v[12:13], v[42:43], s[26:27]
	v_med3_f32 v20, v20, s71, v223
	v_rcp_f32_e32 v14, v14
	v_sub_f32_e32 v8, v8, v9
	v_sub_f32_e32 v12, v12, v13
	v_mul_f32_e32 v16, v16, v20
	v_add_f32_e32 v20, 1.0, v26
	v_max_f32_e32 v8, 0xc1898193, v8
	v_med3_f32 v12, v12, s71, v223
	v_rcp_f32_e32 v20, v20
	v_exp_f32_e32 v27, v8
	v_mul_f32_e32 v8, v8, v12
	v_add_f32_e32 v12, 1.0, v24
	v_add_f32_e32 v24, 1.0, v28
	v_mul_f32_e32 v14, v14, v16
	v_rcp_f32_e32 v16, v24
	v_add_f32_e32 v25, 1.0, v36
	v_mov_b32_e32 v24, v184
	v_sub_f32_e32 v22, v22, v23
	v_pk_mul_f32 v[24:25], v[24:25], s[26:27]
	v_sub_f32_e32 v4, v4, v5
	v_med3_f32 v22, v22, s71, v223
	v_mul_f32_e32 v10, v20, v10
	v_sub_f32_e32 v20, v24, v25
	v_max_f32_e32 v4, 0xc1898193, v4
	v_mul_f32_e32 v18, v18, v22
	v_add_f32_e32 v22, 1.0, v27
	v_med3_f32 v20, v20, s71, v223
	v_add_f32_e32 v27, 1.0, v40
	v_mov_b32_e32 v26, v180
	v_exp_f32_e32 v30, v4
	v_rcp_f32_e32 v12, v12
	v_mul_f32_e32 v6, v6, v20
	v_pk_mul_f32 v[26:27], v[26:27], s[26:27]
	v_rcp_f32_e32 v22, v22
	v_mul_f32_e32 v6, v16, v6
	v_sub_f32_e32 v16, v26, v27
	v_mov_b32_e32 v28, v193
	v_med3_f32 v16, v16, s71, v223
	v_pk_mul_f32 v[28:29], v[28:29], s[24:25]
	v_mul_f32_e32 v4, v4, v16
	v_sub_f32_e32 v16, v28, v29
	v_mov_b32_e32 v32, v189
	v_mul_f32_e32 v12, v12, v18
	v_add_f32_e32 v18, 1.0, v30
	v_max_f32_e32 v16, 0xc1898193, v16
	v_pk_mul_f32 v[30:31], v[32:33], s[24:25]
	v_mul_f32_e32 v8, v22, v8
	v_rcp_f32_e32 v18, v18
	v_sub_f32_e32 v20, v30, v31
	v_exp_f32_e32 v22, v16
	v_max_f32_e32 v20, 0xc1898193, v20
	v_exp_f32_e32 v24, v20
	v_mul_f32_e32 v4, v18, v4
	v_add_f32_e32 v18, 1.0, v22
	v_add_f32_e32 v33, 1.0, v37
	v_mov_b32_e32 v32, v185
	v_rcp_f32_e32 v18, v18
	v_pk_mul_f32 v[32:33], v[32:33], s[26:27]
	v_mov_b32_e32 v36, v199
	v_add_f32_e32 v22, 1.0, v24
	v_sub_f32_e32 v24, v32, v33
	v_cvt_pk_fp8_f32 v36, v12, v10
	v_med3_f32 v24, v24, s71, v223
	v_mul_f32_e32 v16, v16, v24
	v_mul_f32_e32 v16, v18, v16
	v_add_f32_e32 v35, 1.0, v41
	v_mov_b32_e32 v34, v181
	v_cvt_pk_fp8_f32 v36, v6, v16 op_sel:[0,0,1]
	v_fma_f32 v6, v174, s24, -v19
	v_rcp_f32_e32 v22, v22
	v_pk_mul_f32 v[34:35], v[34:35], s[26:27]
	v_mov_b32_e32 v37, v199
	v_max_f32_e32 v6, 0xc1898193, v6
	v_sub_f32_e32 v18, v34, v35
	v_cvt_pk_fp8_f32 v37, v14, v8
	v_exp_f32_e32 v12, v6
	v_med3_f32 v10, v18, s71, v223
	v_mul_f32_e32 v10, v20, v10
	v_mul_f32_e32 v10, v22, v10
	v_cvt_pk_fp8_f32 v37, v4, v10 op_sel:[0,0,1]
	v_add_f32_e32 v4, 1.0, v12
	v_rcp_f32_e32 v4, v4
	v_fma_f32 v8, v170, s24, -v17
	v_fma_f32 v12, v166, s26, -v23
	v_max_f32_e32 v8, 0xc1898193, v8
	v_med3_f32 v12, v12, s71, v223
	v_exp_f32_e32 v14, v8
	v_mul_f32_e32 v6, v6, v12
	v_mul_f32_e32 v4, v4, v6
	v_fma_f32 v6, v162, s26, -v21
	v_med3_f32 v6, v6, s71, v223
	v_mul_f32_e32 v6, v8, v6
	v_fma_f32 v8, v175, s24, -v11
	v_add_f32_e32 v10, 1.0, v14
	v_max_f32_e32 v8, 0xc1898193, v8
	v_rcp_f32_e32 v10, v10
	v_fma_f32 v12, v171, s24, -v9
	v_exp_f32_e32 v14, v8
	v_max_f32_e32 v12, 0xc1898193, v12
	v_exp_f32_e32 v16, v12
	v_mul_f32_e32 v6, v10, v6
	v_add_f32_e32 v10, 1.0, v14
	v_rcp_f32_e32 v10, v10
	v_add_f32_e32 v14, 1.0, v16
	v_fma_f32 v16, v167, s26, -v15
	v_med3_f32 v16, v16, s71, v223
	v_mul_f32_e32 v8, v8, v16
	v_mul_f32_e32 v8, v10, v8
	v_fma_f32 v10, v163, s26, -v13
	v_med3_f32 v10, v10, s71, v223
	v_mul_f32_e32 v10, v12, v10
	v_fma_f32 v12, v176, s24, -v7
	v_max_f32_e32 v12, 0xc1898193, v12
	v_rcp_f32_e32 v14, v14
	v_fma_f32 v16, v172, s24, -v5
	v_exp_f32_e32 v18, v12
	v_max_f32_e32 v16, 0xc1898193, v16
	v_exp_f32_e32 v20, v16
	v_mul_f32_e32 v10, v14, v10
	v_add_f32_e32 v14, 1.0, v18
	v_rcp_f32_e32 v14, v14
	v_add_f32_e32 v18, 1.0, v20
	v_fma_f32 v20, v168, s26, -v25
	v_med3_f32 v20, v20, s71, v223
	v_mul_f32_e32 v12, v12, v20
	v_mul_f32_e32 v12, v14, v12
	v_fma_f32 v14, v164, s26, -v27
	v_med3_f32 v14, v14, s71, v223
	v_mul_f32_e32 v14, v16, v14
	v_fma_f32 v16, v177, s24, -v29
	v_max_f32_e32 v16, 0xc1898193, v16
	v_rcp_f32_e32 v18, v18
	v_fma_f32 v20, v173, s24, -v31
	v_exp_f32_e32 v22, v16
	v_max_f32_e32 v20, 0xc1898193, v20
	v_exp_f32_e32 v24, v20
	v_mul_f32_e32 v14, v18, v14
	v_add_f32_e32 v18, 1.0, v22
	v_rcp_f32_e32 v18, v18
	v_add_f32_e32 v22, 1.0, v24
	v_fma_f32 v24, v169, s26, -v33
	v_med3_f32 v24, v24, s71, v223
	v_rcp_f32_e32 v22, v22
	v_mul_f32_e32 v16, v16, v24
	v_mov_b32_e32 v39, v199
	v_mul_f32_e32 v16, v18, v16
	v_fma_f32 v18, v165, s26, -v35
	v_cvt_pk_fp8_f32 v39, v6, v10
	v_med3_f32 v18, v18, s71, v223
	v_mov_b32_e32 v38, v199
	v_cvt_pk_fp8_f32 v38, v4, v8
	v_mul_f32_e32 v4, v20, v18
	v_mul_f32_e32 v4, v22, v4
	v_cvt_pk_fp8_f32 v39, v14, v4 op_sel:[0,0,1]
	v_fma_f32 v4, v158, s24, -v19
	v_max_f32_e32 v4, 0xc1898193, v4
	v_exp_f32_e32 v8, v4
	v_cvt_pk_fp8_f32 v38, v12, v16 op_sel:[0,0,1]
	v_fma_f32 v6, v154, s24, -v17
	v_fma_f32 v12, v150, s26, -v23
	v_add_f32_e32 v8, 1.0, v8
	v_rcp_f32_e32 v8, v8
	v_max_f32_e32 v6, 0xc1898193, v6
	v_med3_f32 v12, v12, s71, v223
	v_exp_f32_e32 v10, v6
	v_mul_f32_e32 v4, v4, v12
	v_mul_f32_e32 v4, v8, v4
	v_fma_f32 v8, v146, s26, -v21
	v_med3_f32 v8, v8, s71, v223
	v_mul_f32_e32 v6, v6, v8
	v_fma_f32 v8, v159, s24, -v11
	v_add_f32_e32 v10, 1.0, v10
	v_max_f32_e32 v8, 0xc1898193, v8
	v_rcp_f32_e32 v10, v10
	v_fma_f32 v12, v155, s24, -v9
	v_exp_f32_e32 v14, v8
	v_max_f32_e32 v12, 0xc1898193, v12
	v_exp_f32_e32 v16, v12
	v_mul_f32_e32 v6, v10, v6
	v_add_f32_e32 v10, 1.0, v14
	v_rcp_f32_e32 v10, v10
	v_add_f32_e32 v14, 1.0, v16
	v_fma_f32 v16, v151, s26, -v15
	v_med3_f32 v16, v16, s71, v223
	v_mul_f32_e32 v8, v8, v16
	v_mul_f32_e32 v8, v10, v8
	v_fma_f32 v10, v147, s26, -v13
	v_med3_f32 v10, v10, s71, v223
	v_mul_f32_e32 v10, v12, v10
	v_fma_f32 v12, v160, s24, -v7
	v_max_f32_e32 v12, 0xc1898193, v12
	v_rcp_f32_e32 v14, v14
	v_fma_f32 v16, v156, s24, -v5
	v_exp_f32_e32 v18, v12
	v_max_f32_e32 v16, 0xc1898193, v16
	v_exp_f32_e32 v20, v16
	v_mul_f32_e32 v10, v14, v10
	v_add_f32_e32 v14, 1.0, v18
	v_rcp_f32_e32 v14, v14
	v_add_f32_e32 v18, 1.0, v20
	v_fma_f32 v20, v152, s26, -v25
	v_med3_f32 v20, v20, s71, v223
	v_mul_f32_e32 v12, v12, v20
	v_mul_f32_e32 v12, v14, v12
	v_fma_f32 v14, v148, s26, -v27
	v_med3_f32 v14, v14, s71, v223
	v_mul_f32_e32 v14, v16, v14
	v_fma_f32 v16, v161, s24, -v29
	v_max_f32_e32 v16, 0xc1898193, v16
	v_rcp_f32_e32 v18, v18
	v_fma_f32 v20, v157, s24, -v31
	v_exp_f32_e32 v22, v16
	v_max_f32_e32 v20, 0xc1898193, v20
	v_exp_f32_e32 v24, v20
	v_mul_f32_e32 v14, v18, v14
	v_add_f32_e32 v18, 1.0, v22
	v_permlane16_swap_b32_e32 v36, v38
	v_permlane16_swap_b32_e32 v37, v39
	v_rcp_f32_e32 v18, v18
	global_store_dwordx4 v[2:3], v[36:39], off
	v_add_f32_e32 v22, 1.0, v24
	v_fma_f32 v24, v153, s26, -v33
	v_mov_b32_e32 v36, v199
	v_mov_b32_e32 v37, v199
	v_med3_f32 v24, v24, s71, v223
	v_cvt_pk_fp8_f32 v36, v4, v8
	v_cvt_pk_fp8_f32 v37, v6, v10
	v_fma_f32 v6, v142, s24, -v19
	v_rcp_f32_e32 v22, v22
	v_mul_f32_e32 v16, v16, v24
	v_max_f32_e32 v6, 0xc1898193, v6
	v_mul_f32_e32 v16, v18, v16
	v_fma_f32 v18, v149, s26, -v35
	v_fma_f32 v8, v138, s24, -v17
	v_exp_f32_e32 v10, v6
	v_med3_f32 v4, v18, s71, v223
	v_max_f32_e32 v8, 0xc1898193, v8
	v_mul_f32_e32 v4, v20, v4
	v_cvt_pk_fp8_f32 v36, v12, v16 op_sel:[0,0,1]
	v_exp_f32_e32 v12, v8
	v_mul_f32_e32 v4, v22, v4
	v_cvt_pk_fp8_f32 v37, v14, v4 op_sel:[0,0,1]
	v_add_f32_e32 v4, 1.0, v10
	v_rcp_f32_e32 v4, v4
	v_add_f32_e32 v10, 1.0, v12
	v_fma_f32 v12, v134, s26, -v23
	v_med3_f32 v12, v12, s71, v223
	v_mul_f32_e32 v6, v6, v12
	v_mul_f32_e32 v4, v4, v6
	v_fma_f32 v6, v130, s26, -v21
	v_med3_f32 v6, v6, s71, v223
	v_mul_f32_e32 v6, v8, v6
	v_fma_f32 v8, v143, s24, -v11
	v_max_f32_e32 v8, 0xc1898193, v8
	v_rcp_f32_e32 v10, v10
	v_fma_f32 v12, v139, s24, -v9
	v_exp_f32_e32 v14, v8
	v_max_f32_e32 v12, 0xc1898193, v12
	v_exp_f32_e32 v16, v12
	v_mul_f32_e32 v6, v10, v6
	v_add_f32_e32 v10, 1.0, v14
	v_rcp_f32_e32 v10, v10
	v_add_f32_e32 v14, 1.0, v16
	v_fma_f32 v16, v135, s26, -v15
	v_med3_f32 v16, v16, s71, v223
	v_mul_f32_e32 v8, v8, v16
	v_mul_f32_e32 v8, v10, v8
	v_fma_f32 v10, v131, s26, -v13
	v_med3_f32 v10, v10, s71, v223
	v_mul_f32_e32 v10, v12, v10
	v_fma_f32 v12, v144, s24, -v7
	v_max_f32_e32 v12, 0xc1898193, v12
	v_rcp_f32_e32 v14, v14
	v_fma_f32 v16, v140, s24, -v5
	v_exp_f32_e32 v18, v12
	v_max_f32_e32 v16, 0xc1898193, v16
	v_exp_f32_e32 v20, v16
	v_mul_f32_e32 v10, v14, v10
	v_add_f32_e32 v14, 1.0, v18
	v_rcp_f32_e32 v14, v14
	v_add_f32_e32 v18, 1.0, v20
	v_fma_f32 v20, v136, s26, -v25
	v_med3_f32 v20, v20, s71, v223
	v_mul_f32_e32 v12, v12, v20
	v_mul_f32_e32 v12, v14, v12
	v_fma_f32 v14, v132, s26, -v27
	v_med3_f32 v14, v14, s71, v223
	v_mul_f32_e32 v14, v16, v14
	v_fma_f32 v16, v145, s24, -v29
	v_max_f32_e32 v16, 0xc1898193, v16
	v_rcp_f32_e32 v18, v18
	v_fma_f32 v20, v141, s24, -v31
	v_exp_f32_e32 v22, v16
	v_max_f32_e32 v20, 0xc1898193, v20
	v_exp_f32_e32 v24, v20
	v_mul_f32_e32 v14, v18, v14
	v_add_f32_e32 v18, 1.0, v22
	v_rcp_f32_e32 v18, v18
	v_add_f32_e32 v22, 1.0, v24
	v_fma_f32 v24, v137, s26, -v33
	v_med3_f32 v24, v24, s71, v223
	v_rcp_f32_e32 v22, v22
	v_mul_f32_e32 v16, v16, v24
	v_mov_b32_e32 v39, v199
	v_mul_f32_e32 v16, v18, v16
	v_fma_f32 v18, v133, s26, -v35
	v_cvt_pk_fp8_f32 v39, v6, v10
	v_med3_f32 v18, v18, s71, v223
	v_mov_b32_e32 v38, v199
	v_cvt_pk_fp8_f32 v38, v4, v8
	v_mul_f32_e32 v4, v20, v18
	v_mul_f32_e32 v4, v22, v4
	v_cvt_pk_fp8_f32 v39, v14, v4 op_sel:[0,0,1]
	v_fma_f32 v4, v126, s24, -v19
	v_max_f32_e32 v4, 0xc1898193, v4
	v_exp_f32_e32 v8, v4
	v_cvt_pk_fp8_f32 v38, v12, v16 op_sel:[0,0,1]
	v_fma_f32 v6, v122, s24, -v17
	v_fma_f32 v12, v118, s26, -v23
	v_add_f32_e32 v8, 1.0, v8
	v_rcp_f32_e32 v8, v8
	v_max_f32_e32 v6, 0xc1898193, v6
	v_med3_f32 v12, v12, s71, v223
	v_exp_f32_e32 v10, v6
	v_mul_f32_e32 v4, v4, v12
	v_mul_f32_e32 v4, v8, v4
	v_fma_f32 v8, v114, s26, -v21
	v_med3_f32 v8, v8, s71, v223
	v_mul_f32_e32 v6, v6, v8
	v_fma_f32 v8, v127, s24, -v11
	v_add_f32_e32 v10, 1.0, v10
	v_max_f32_e32 v8, 0xc1898193, v8
	v_rcp_f32_e32 v10, v10
	v_fma_f32 v12, v123, s24, -v9
	v_exp_f32_e32 v14, v8
	v_max_f32_e32 v12, 0xc1898193, v12
	v_exp_f32_e32 v16, v12
	v_mul_f32_e32 v6, v10, v6
	v_add_f32_e32 v10, 1.0, v14
	v_rcp_f32_e32 v10, v10
	v_add_f32_e32 v14, 1.0, v16
	v_fma_f32 v16, v119, s26, -v15
	v_med3_f32 v16, v16, s71, v223
	v_mul_f32_e32 v8, v8, v16
	v_mul_f32_e32 v8, v10, v8
	v_fma_f32 v10, v115, s26, -v13
	v_med3_f32 v10, v10, s71, v223
	v_mul_f32_e32 v10, v12, v10
	v_fma_f32 v12, v128, s24, -v7
	v_max_f32_e32 v12, 0xc1898193, v12
	v_rcp_f32_e32 v14, v14
	v_fma_f32 v16, v124, s24, -v5
	v_exp_f32_e32 v18, v12
	v_max_f32_e32 v16, 0xc1898193, v16
	v_exp_f32_e32 v20, v16
	v_mul_f32_e32 v10, v14, v10
	v_add_f32_e32 v14, 1.0, v18
	v_rcp_f32_e32 v14, v14
	v_add_f32_e32 v18, 1.0, v20
	v_fma_f32 v20, v120, s26, -v25
	v_med3_f32 v20, v20, s71, v223
	v_mul_f32_e32 v12, v12, v20
	v_mul_f32_e32 v12, v14, v12
	v_fma_f32 v14, v116, s26, -v27
	v_med3_f32 v14, v14, s71, v223
	v_mul_f32_e32 v14, v16, v14
	v_fma_f32 v16, v129, s24, -v29
	v_max_f32_e32 v16, 0xc1898193, v16
	v_rcp_f32_e32 v18, v18
	v_fma_f32 v20, v125, s24, -v31
	v_exp_f32_e32 v22, v16
	v_max_f32_e32 v20, 0xc1898193, v20
	v_exp_f32_e32 v24, v20
	v_add_co_u32_e32 v40, vcc, s2, v2
	v_mul_f32_e32 v14, v18, v14
	v_add_f32_e32 v18, 1.0, v22
	v_permlane16_swap_b32_e32 v36, v38
	v_permlane16_swap_b32_e32 v37, v39
	v_addc_co_u32_e32 v41, vcc, 0, v3, vcc
	v_rcp_f32_e32 v18, v18
	global_store_dwordx4 v[40:41], v[36:39], off
	v_add_f32_e32 v22, 1.0, v24
	v_fma_f32 v24, v121, s26, -v33
	v_mov_b32_e32 v36, v199
	v_mov_b32_e32 v37, v199
	v_med3_f32 v24, v24, s71, v223
	v_cvt_pk_fp8_f32 v36, v4, v8
	v_cvt_pk_fp8_f32 v37, v6, v10
	v_fma_f32 v6, v110, s24, -v19
	v_rcp_f32_e32 v22, v22
	v_mul_f32_e32 v16, v16, v24
	v_max_f32_e32 v6, 0xc1898193, v6
	v_mul_f32_e32 v16, v18, v16
	v_fma_f32 v18, v117, s26, -v35
	v_fma_f32 v8, v106, s24, -v17
	v_exp_f32_e32 v10, v6
	v_med3_f32 v4, v18, s71, v223
	v_max_f32_e32 v8, 0xc1898193, v8
	v_mul_f32_e32 v4, v20, v4
	v_cvt_pk_fp8_f32 v36, v12, v16 op_sel:[0,0,1]
	v_exp_f32_e32 v12, v8
	v_mul_f32_e32 v4, v22, v4
	v_cvt_pk_fp8_f32 v37, v14, v4 op_sel:[0,0,1]
	v_add_f32_e32 v4, 1.0, v10
	v_rcp_f32_e32 v4, v4
	v_add_f32_e32 v10, 1.0, v12
	v_fma_f32 v12, v102, s26, -v23
	v_med3_f32 v12, v12, s71, v223
	v_mul_f32_e32 v6, v6, v12
	v_mul_f32_e32 v4, v4, v6
	v_fma_f32 v6, v90, s26, -v21
	v_med3_f32 v6, v6, s71, v223
	v_mul_f32_e32 v6, v8, v6
	v_fma_f32 v8, v111, s24, -v11
	v_max_f32_e32 v8, 0xc1898193, v8
	v_rcp_f32_e32 v10, v10
	v_fma_f32 v12, v107, s24, -v9
	v_exp_f32_e32 v14, v8
	v_max_f32_e32 v12, 0xc1898193, v12
	v_exp_f32_e32 v16, v12
	v_mul_f32_e32 v6, v10, v6
	v_add_f32_e32 v10, 1.0, v14
	v_rcp_f32_e32 v10, v10
	v_add_f32_e32 v14, 1.0, v16
	v_fma_f32 v16, v103, s26, -v15
	v_med3_f32 v16, v16, s71, v223
	v_mul_f32_e32 v8, v8, v16
	v_mul_f32_e32 v8, v10, v8
	v_fma_f32 v10, v91, s26, -v13
	v_med3_f32 v10, v10, s71, v223
	v_mul_f32_e32 v10, v12, v10
	v_fma_f32 v12, v112, s24, -v7
	v_max_f32_e32 v12, 0xc1898193, v12
	v_rcp_f32_e32 v14, v14
	v_fma_f32 v16, v108, s24, -v5
	v_exp_f32_e32 v18, v12
	v_max_f32_e32 v16, 0xc1898193, v16
	v_exp_f32_e32 v20, v16
	v_mul_f32_e32 v10, v14, v10
	v_add_f32_e32 v14, 1.0, v18
	v_rcp_f32_e32 v14, v14
	v_add_f32_e32 v18, 1.0, v20
	v_fma_f32 v20, v104, s26, -v25
	v_med3_f32 v20, v20, s71, v223
	v_mul_f32_e32 v12, v12, v20
	v_mul_f32_e32 v12, v14, v12
	v_fma_f32 v14, v92, s26, -v27
	v_med3_f32 v14, v14, s71, v223
	v_mul_f32_e32 v14, v16, v14
	v_fma_f32 v16, v113, s24, -v29
	v_max_f32_e32 v16, 0xc1898193, v16
	v_rcp_f32_e32 v18, v18
	v_fma_f32 v20, v109, s24, -v31
	v_exp_f32_e32 v22, v16
	v_max_f32_e32 v20, 0xc1898193, v20
	v_exp_f32_e32 v24, v20
	v_mul_f32_e32 v14, v18, v14
	v_add_f32_e32 v18, 1.0, v22
	v_rcp_f32_e32 v18, v18
	v_add_f32_e32 v22, 1.0, v24
	v_fma_f32 v24, v105, s26, -v33
	v_med3_f32 v24, v24, s71, v223
	v_rcp_f32_e32 v22, v22
	v_mul_f32_e32 v16, v16, v24
	v_mov_b32_e32 v39, v199
	v_mul_f32_e32 v16, v18, v16
	v_fma_f32 v18, v93, s26, -v35
	v_cvt_pk_fp8_f32 v39, v6, v10
	v_med3_f32 v18, v18, s71, v223
	v_mov_b32_e32 v38, v199
	v_cvt_pk_fp8_f32 v38, v4, v8
	v_mul_f32_e32 v4, v20, v18
	v_mul_f32_e32 v4, v22, v4
	v_cvt_pk_fp8_f32 v39, v14, v4 op_sel:[0,0,1]
	v_fma_f32 v4, v86, s24, -v19
	v_max_f32_e32 v4, 0xc1898193, v4
	v_exp_f32_e32 v8, v4
	v_cvt_pk_fp8_f32 v38, v12, v16 op_sel:[0,0,1]
	v_fma_f32 v6, v82, s24, -v17
	v_fma_f32 v12, v94, s26, -v23
	v_add_f32_e32 v8, 1.0, v8
	v_rcp_f32_e32 v8, v8
	v_max_f32_e32 v6, 0xc1898193, v6
	v_med3_f32 v12, v12, s71, v223
	v_exp_f32_e32 v10, v6
	v_mul_f32_e32 v4, v4, v12
	v_mul_f32_e32 v4, v8, v4
	v_fma_f32 v8, v98, s26, -v21
	v_med3_f32 v8, v8, s71, v223
	v_mul_f32_e32 v6, v6, v8
	v_fma_f32 v8, v87, s24, -v11
	v_add_f32_e32 v10, 1.0, v10
	v_max_f32_e32 v8, 0xc1898193, v8
	v_rcp_f32_e32 v10, v10
	v_fma_f32 v12, v83, s24, -v9
	v_exp_f32_e32 v14, v8
	v_max_f32_e32 v12, 0xc1898193, v12
	v_exp_f32_e32 v16, v12
	v_mul_f32_e32 v6, v10, v6
	v_add_f32_e32 v10, 1.0, v14
	v_rcp_f32_e32 v10, v10
	v_add_f32_e32 v14, 1.0, v16
	v_fma_f32 v16, v95, s26, -v15
	v_med3_f32 v16, v16, s71, v223
	v_mul_f32_e32 v8, v8, v16
	v_mul_f32_e32 v8, v10, v8
	v_fma_f32 v10, v99, s26, -v13
	v_med3_f32 v10, v10, s71, v223
	v_mul_f32_e32 v10, v12, v10
	v_fma_f32 v12, v88, s24, -v7
	v_max_f32_e32 v12, 0xc1898193, v12
	v_rcp_f32_e32 v14, v14
	v_fma_f32 v16, v84, s24, -v5
	v_exp_f32_e32 v18, v12
	v_max_f32_e32 v16, 0xc1898193, v16
	v_exp_f32_e32 v20, v16
	v_mul_f32_e32 v10, v14, v10
	v_add_f32_e32 v14, 1.0, v18
	v_rcp_f32_e32 v14, v14
	v_add_f32_e32 v18, 1.0, v20
	v_fma_f32 v20, v96, s26, -v25
	v_med3_f32 v20, v20, s71, v223
	v_mul_f32_e32 v12, v12, v20
	v_mul_f32_e32 v12, v14, v12
	v_fma_f32 v14, v100, s26, -v27
	v_med3_f32 v14, v14, s71, v223
	v_mul_f32_e32 v14, v16, v14
	v_fma_f32 v16, v89, s24, -v29
	v_max_f32_e32 v16, 0xc1898193, v16
	v_rcp_f32_e32 v18, v18
	v_fma_f32 v20, v85, s24, -v31
	v_exp_f32_e32 v22, v16
	v_max_f32_e32 v20, 0xc1898193, v20
	v_exp_f32_e32 v24, v20
	s_mov_b32 s2, 0x20000
	v_add_co_u32_e32 v40, vcc, s2, v2
	v_mul_f32_e32 v14, v18, v14
	v_add_f32_e32 v18, 1.0, v22
	v_permlane16_swap_b32_e32 v36, v38
	v_permlane16_swap_b32_e32 v37, v39
	v_addc_co_u32_e32 v41, vcc, 0, v3, vcc
	v_rcp_f32_e32 v18, v18
	global_store_dwordx4 v[40:41], v[36:39], off
	v_add_f32_e32 v22, 1.0, v24
	v_fma_f32 v24, v97, s26, -v33
	v_mov_b32_e32 v36, v199
	v_mov_b32_e32 v37, v199
	v_med3_f32 v24, v24, s71, v223
	v_cvt_pk_fp8_f32 v36, v4, v8
	v_cvt_pk_fp8_f32 v37, v6, v10
	v_fma_f32 v6, v70, s24, -v19
	v_rcp_f32_e32 v22, v22
	v_mul_f32_e32 v16, v16, v24
	v_max_f32_e32 v6, 0xc1898193, v6
	v_mul_f32_e32 v16, v18, v16
	v_fma_f32 v18, v101, s26, -v35
	v_fma_f32 v8, v66, s24, -v17
	v_exp_f32_e32 v10, v6
	v_med3_f32 v4, v18, s71, v223
	v_max_f32_e32 v8, 0xc1898193, v8
	v_mul_f32_e32 v4, v20, v4
	v_cvt_pk_fp8_f32 v36, v12, v16 op_sel:[0,0,1]
	v_exp_f32_e32 v12, v8
	v_mul_f32_e32 v4, v22, v4
	v_cvt_pk_fp8_f32 v37, v14, v4 op_sel:[0,0,1]
	v_add_f32_e32 v4, 1.0, v10
	v_rcp_f32_e32 v4, v4
	v_add_f32_e32 v10, 1.0, v12
	v_fma_f32 v12, v74, s26, -v23
	v_med3_f32 v12, v12, s71, v223
	v_mul_f32_e32 v6, v6, v12
	v_mul_f32_e32 v4, v4, v6
	v_fma_f32 v6, v78, s26, -v21
	v_med3_f32 v6, v6, s71, v223
	v_mul_f32_e32 v6, v8, v6
	v_fma_f32 v8, v71, s24, -v11
	v_max_f32_e32 v8, 0xc1898193, v8
	v_rcp_f32_e32 v10, v10
	v_fma_f32 v9, v67, s24, -v9
	v_exp_f32_e32 v11, v8
	v_max_f32_e32 v9, 0xc1898193, v9
	v_exp_f32_e32 v12, v9
	v_mul_f32_e32 v6, v10, v6
	v_add_f32_e32 v10, 1.0, v11
	v_rcp_f32_e32 v10, v10
	v_add_f32_e32 v11, 1.0, v12
	v_fma_f32 v12, v75, s26, -v15
	v_med3_f32 v12, v12, s71, v223
	v_mul_f32_e32 v8, v8, v12
	v_mul_f32_e32 v8, v10, v8
	v_fma_f32 v10, v79, s26, -v13
	v_fma_f32 v7, v72, s24, -v7
	v_med3_f32 v10, v10, s71, v223
	v_max_f32_e32 v7, 0xc1898193, v7
	v_mul_f32_e32 v9, v9, v10
	v_fma_f32 v5, v68, s24, -v5
	v_exp_f32_e32 v10, v7
	v_max_f32_e32 v5, 0xc1898193, v5
	v_rcp_f32_e32 v11, v11
	v_exp_f32_e32 v12, v5
	v_add_f32_e32 v10, 1.0, v10
	v_rcp_f32_e32 v10, v10
	v_mul_f32_e32 v9, v11, v9
	v_add_f32_e32 v11, 1.0, v12
	v_fma_f32 v12, v76, s26, -v25
	v_med3_f32 v12, v12, s71, v223
	v_mul_f32_e32 v7, v7, v12
	v_mul_f32_e32 v7, v10, v7
	v_fma_f32 v10, v80, s26, -v27
	v_med3_f32 v10, v10, s71, v223
	v_mul_f32_e32 v5, v5, v10
	v_fma_f32 v10, v73, s24, -v29
	v_max_f32_e32 v10, 0xc1898193, v10
	v_rcp_f32_e32 v11, v11
	v_fma_f32 v12, v69, s24, -v31
	v_exp_f32_e32 v13, v10
	v_max_f32_e32 v12, 0xc1898193, v12
	v_exp_f32_e32 v14, v12
	v_mul_f32_e32 v5, v11, v5
	v_add_f32_e32 v11, 1.0, v13
	v_rcp_f32_e32 v11, v11
	v_add_f32_e32 v13, 1.0, v14
	v_fma_f32 v14, v77, s26, -v33
	v_med3_f32 v14, v14, s71, v223
	v_rcp_f32_e32 v13, v13
	v_mul_f32_e32 v10, v10, v14
	v_mov_b32_e32 v38, v199
	v_mov_b32_e32 v39, v199
	v_mul_f32_e32 v10, v11, v10
	v_fma_f32 v11, v81, s26, -v35
	v_cvt_pk_fp8_f32 v38, v4, v8
	v_cvt_pk_fp8_f32 v39, v6, v9
	v_med3_f32 v11, v11, s71, v223
	v_mul_f32_e32 v4, v12, v11
	v_mul_f32_e32 v4, v13, v4
	v_cvt_pk_fp8_f32 v38, v7, v10 op_sel:[0,0,1]
	v_cvt_pk_fp8_f32 v39, v5, v4 op_sel:[0,0,1]
	v_add_co_u32_e32 v2, vcc, 0x28000, v2
	v_permlane16_swap_b32_e32 v36, v38
	s_nop 0
	v_addc_co_u32_e32 v3, vcc, 0, v3, vcc
	v_permlane16_swap_b32_e32 v37, v39
	s_and_b64 vcc, exec, s[4:5]
	s_mov_b64 s[4:5], -1
	global_store_dwordx4 v[2:3], v[36:39], off
	s_cbranch_vccnz .LBB0_975
	s_andn2_b64 vcc, exec, s[16:17]
	s_cbranch_vccnz .LBB0_974
	s_barrier
	s_branch .LBB0_974

	.amdhsa_kernel _Z6mk_fwd4Args
		.amdhsa_group_segment_fixed_size 0
		.amdhsa_private_segment_fixed_size 0
		.amdhsa_kernarg_size 416
		.amdhsa_user_sgpr_count 2
		.amdhsa_user_sgpr_dispatch_ptr 0
		.amdhsa_user_sgpr_queue_ptr 0
		.amdhsa_user_sgpr_kernarg_segment_ptr 1
		.amdhsa_user_sgpr_dispatch_id 0
		.amdhsa_user_sgpr_kernarg_preload_length 0
		.amdhsa_user_sgpr_kernarg_preload_offset 0
		.amdhsa_user_sgpr_private_segment_size 0
		.amdhsa_uses_dynamic_stack 0
		.amdhsa_enable_private_segment 0
		.amdhsa_system_sgpr_workgroup_id_x 1
		.amdhsa_system_sgpr_workgroup_id_y 0
		.amdhsa_system_sgpr_workgroup_id_z 0
		.amdhsa_system_sgpr_workgroup_info 0
		.amdhsa_system_vgpr_workitem_id 0
		.amdhsa_next_free_vgpr 256
		.amdhsa_next_free_sgpr 102
		.amdhsa_accum_offset 256
		.amdhsa_reserve_vcc 1
		.amdhsa_float_round_mode_32 0
		.amdhsa_float_round_mode_16_64 0
		.amdhsa_float_denorm_mode_32 3
		.amdhsa_float_denorm_mode_16_64 3
		.amdhsa_dx10_clamp 1
		.amdhsa_ieee_mode 1
		.amdhsa_fp16_overflow 0
		.amdhsa_tg_split 0
		.amdhsa_exception_fp_ieee_invalid_op 0
		.amdhsa_exception_fp_denorm_src 0
		.amdhsa_exception_fp_ieee_div_zero 0
		.amdhsa_exception_fp_ieee_overflow 0
		.amdhsa_exception_fp_ieee_underflow 0
		.amdhsa_exception_fp_ieee_inexact 0
		.amdhsa_exception_int_div_zero 0
	.end_amdhsa_kernel

amdhsa.kernels:
  - .agpr_count:     0
    .args:
      - .offset:         0
        .size:           160
        .value_kind:     by_value
      - .offset:         160
        .size:           4
        .value_kind:     hidden_block_count_x
      - .offset:         164
        .size:           4
        .value_kind:     hidden_block_count_y
      - .offset:         168
        .size:           4
        .value_kind:     hidden_block_count_z
      - .offset:         172
        .size:           2
        .value_kind:     hidden_group_size_x
      - .offset:         174
        .size:           2
        .value_kind:     hidden_group_size_y
      - .offset:         176
        .size:           2
        .value_kind:     hidden_group_size_z
      - .offset:         178
        .size:           2
        .value_kind:     hidden_remainder_x
      - .offset:         180
        .size:           2
        .value_kind:     hidden_remainder_y
      - .offset:         182
        .size:           2
        .value_kind:     hidden_remainder_z
      - .offset:         200
        .size:           8
        .value_kind:     hidden_global_offset_x
      - .offset:         208
        .size:           8
        .value_kind:     hidden_global_offset_y
      - .offset:         216
        .size:           8
        .value_kind:     hidden_global_offset_z
      - .offset:         224
        .size:           2
        .value_kind:     hidden_grid_dims
      - .offset:         280
        .size:           4
        .value_kind:     hidden_dynamic_lds_size
    .group_segment_fixed_size: 0
    .kernarg_segment_align: 8
    .kernarg_segment_size: 416
    .language:       OpenCL C
    .language_version:
      - 2
      - 0
    .max_flat_workgroup_size: 512
    .name:           _Z6mk_fwd4Args
    .private_segment_fixed_size: 0
    .sgpr_count:     108
    .sgpr_spill_count: 115
    .symbol:         _Z6mk_fwd4Args.kd
    .uniform_work_group_size: 1
    .uses_dynamic_stack: false
    .vgpr_count:     256
    .vgpr_spill_count: 0
    .wavefront_size: 64
